# no per-phase setprio flips in the gate-up GEMM loop (on top of peel + dma hoist + pk split)
# baseline (speedup 1.0000x reference)
.LBB0_1549:
	s_ashr_i32 s25, s15, 31
	s_mov_b32 s24, s15
	s_lshl_b64 s[24:25], s[24:25], 19
	s_add_u32 s24, s16, s24
	s_addc_u32 s25, s17, s25
	s_and_b64 vcc, exec, s[10:11]
	s_cbranch_vccnz .LBB0_1545
	s_and_b64 s[30:31], s[26:27], exec
	s_cselect_b32 s67, s25, s29
	s_cselect_b32 s68, s24, s28
	s_lshl_b32 s30, s64, 11
	s_add_i32 s30, s30, 0
	s_add_i32 s30, s30, 0x20400
	s_add_u32 s69, s28, 0x100
	v_mov_b32_e32 v50, 0
	v_add3_u32 v179, s30, v198, v199
	v_add3_u32 v180, s30, v200, v201
	s_addc_u32 s70, s29, 0
	s_mov_b32 s71, 0
	s_mov_b64 s[28:29], 0
	ds_read_b128 v[2:5], v206
	ds_read_b128 v[10:13], v206 offset:2048
	ds_read_b128 v[6:9], v207
	ds_read_b128 v[14:17], v207 offset:2048
	s_cmp_eq_u32 s51, s71
	s_cselect_b64 s[34:35], -1, 0
	s_add_u32 s30, s53, s28
	s_addc_u32 s31, s54, s29
	s_mov_b32 m0, s55
	ds_read_b128 v[26:29], v208
	ds_read_b128 v[18:21], v208 offset:2048
	ds_read_b128 v[30:33], v209
	ds_read_b128 v[22:25], v209 offset:2048
	ds_read_b128 v[42:45], v208 offset:4096
	ds_read_b128 v[34:37], v208 offset:6144
	ds_read_b128 v[46:49], v209 offset:4096
	ds_read_b128 v[38:41], v209 offset:6144
	global_load_lds_dwordx4 v192, s[30:31]
	s_mov_b32 m0, s56
	s_nop 0
	global_load_lds_dwordx4 v194, s[30:31]
	s_waitcnt lgkmcnt(8)
	s_barrier
	s_waitcnt lgkmcnt(0)
	s_barrier
	s_and_b64 s[30:31], s[26:27], s[34:35]
	s_andn2_b64 vcc, exec, s[30:31]
	s_cbranch_vccnz .Lmy_pl2_1553
	ds_read2st64_b32 v[190:191], v179 offset1:2
	ds_read2st64_b32 v[192:193], v180 offset1:2
	s_waitcnt lgkmcnt(0)
	v_add_u32_e32 v184, v190, v1
	v_add_u32_e32 v190, v192, v181
	v_add_u32_e32 v192, v191, v1
	v_add_u32_e32 v194, v193, v181
.Lmy_pl2_1553:
	s_add_i32 s71, s71, 2
	s_add_u32 s30, s28, 0x100
	s_addc_u32 s31, s29, 0
	s_and_b64 s[36:37], s[34:35], exec
	s_cselect_b32 s36, 0, s30
	s_cselect_b32 s37, 0, s31
	s_add_u32 s36, s22, s36
	s_addc_u32 s37, s23, s37
	s_add_u32 s72, s69, s28
	s_addc_u32 s73, s70, s29
	s_and_b64 s[28:29], s[34:35], exec
	s_cselect_b32 s29, s67, s73
	s_cselect_b32 s28, s68, s72
	s_mov_b32 m0, s42
	v_add_u32_e32 v191, s57, v204
	v_lshl_add_u64 v[230:231], s[28:29], 0, v[188:189]
	v_add_u32_e32 v197, s57, v205
	ds_read_b128 v[214:217], v191
	ds_read_b128 v[222:225], v191 offset:2048
	ds_read_b128 v[218:221], v197
	ds_read_b128 v[226:229], v197 offset:2048
	global_load_lds_dwordx4 v[230:231], off
	v_lshl_add_u64 v[232:233], s[28:29], 0, v[186:187]
	s_mov_b32 m0, s43
	s_waitcnt lgkmcnt(0)
	v_mfma_scale_f32_16x16x128_f8f6f4 v[174:177], v[2:9], v[26:33], 0, v211, v210 op_sel_hi:[0,0,0]
	global_load_lds_dwordx4 v[232:233], off
	s_barrier
	s_waitcnt lgkmcnt(0)
	v_mov_b32_e32 v193, v185
	v_mov_b32_e32 v195, v185
	v_mfma_scale_f32_16x16x128_f8f6f4 v[170:173], v[10:17], v[26:33], 0, v211, v210 op_sel_hi:[0,0,0]
	v_mfma_scale_f32_16x16x128_f8f6f4 v[166:169], v[2:9], v[18:25], 0, v211, v210 op_sel_hi:[0,0,0]
	v_mfma_scale_f32_16x16x128_f8f6f4 v[162:165], v[10:17], v[18:25], 0, v211, v210 op_sel_hi:[0,0,0]
	v_mfma_scale_f32_16x16x128_f8f6f4 v[142:145], v[2:9], v[42:49], 0, v211, v210 op_sel_hi:[0,0,0]
	v_mfma_scale_f32_16x16x128_f8f6f4 v[130:133], v[10:17], v[42:49], 0, v211, v210 op_sel_hi:[0,0,0]
	v_mfma_scale_f32_16x16x128_f8f6f4 v[118:121], v[2:9], v[34:41], 0, v211, v210 op_sel_hi:[0,0,0]
	v_mfma_scale_f32_16x16x128_f8f6f4 v[114:117], v[10:17], v[34:41], 0, v211, v210 op_sel_hi:[0,0,0]
	v_mfma_scale_f32_16x16x128_f8f6f4 v[158:161], v[214:221], v[26:33], 0, v211, v210 op_sel_hi:[0,0,0]
	v_mfma_scale_f32_16x16x128_f8f6f4 v[154:157], v[222:229], v[26:33], 0, v211, v210 op_sel_hi:[0,0,0]
	v_mfma_scale_f32_16x16x128_f8f6f4 v[150:153], v[214:221], v[18:25], 0, v211, v210 op_sel_hi:[0,0,0]
	v_mfma_scale_f32_16x16x128_f8f6f4 v[146:149], v[222:229], v[18:25], 0, v211, v210 op_sel_hi:[0,0,0]
	v_mfma_scale_f32_16x16x128_f8f6f4 v[138:141], v[214:221], v[42:49], 0, v211, v210 op_sel_hi:[0,0,0]
	v_mfma_scale_f32_16x16x128_f8f6f4 v[134:137], v[222:229], v[42:49], 0, v211, v210 op_sel_hi:[0,0,0]
	v_mfma_scale_f32_16x16x128_f8f6f4 v[126:129], v[214:221], v[34:41], 0, v211, v210 op_sel_hi:[0,0,0]
	v_mfma_scale_f32_16x16x128_f8f6f4 v[122:125], v[222:229], v[34:41], 0, v211, v210 op_sel_hi:[0,0,0]
	s_mov_b32 m0, s41
	s_barrier
	ds_read_b128 v[18:21], v208 offset:16384
	ds_read_b128 v[26:29], v208 offset:18432
	ds_read_b128 v[22:25], v209 offset:16384
	ds_read_b128 v[30:33], v209 offset:18432
	ds_read_b128 v[34:37], v208 offset:20480
	ds_read_b128 v[42:45], v208 offset:22528
	ds_read_b128 v[38:41], v209 offset:20480
	ds_read_b128 v[46:49], v209 offset:22528
	global_load_lds_dwordx4 v184, s[36:37]
	s_mov_b32 m0, s44
	v_mov_b32_e32 v191, v185
	global_load_lds_dwordx4 v190, s[36:37]
	s_barrier
	s_waitcnt lgkmcnt(0)
	v_lshl_add_u64 v[234:235], s[36:37], 0, v[184:185]
	v_lshl_add_u64 v[236:237], s[36:37], 0, v[190:191]
	s_waitcnt lgkmcnt(0)
	v_mfma_scale_f32_16x16x128_f8f6f4 v[110:113], v[2:9], v[18:25], 0, v211, v210 op_sel_hi:[0,0,0]
	v_mfma_scale_f32_16x16x128_f8f6f4 v[102:105], v[10:17], v[18:25], 0, v211, v210 op_sel_hi:[0,0,0]
	v_mfma_scale_f32_16x16x128_f8f6f4 v[94:97], v[2:9], v[26:33], 0, v211, v210 op_sel_hi:[0,0,0]
	v_mfma_scale_f32_16x16x128_f8f6f4 v[86:89], v[10:17], v[26:33], 0, v211, v210 op_sel_hi:[0,0,0]
	v_mfma_scale_f32_16x16x128_f8f6f4 v[78:81], v[2:9], v[34:41], 0, v211, v210 op_sel_hi:[0,0,0]
	v_mfma_scale_f32_16x16x128_f8f6f4 v[70:73], v[10:17], v[34:41], 0, v211, v210 op_sel_hi:[0,0,0]
	v_mfma_scale_f32_16x16x128_f8f6f4 v[62:65], v[2:9], v[42:49], 0, v211, v210 op_sel_hi:[0,0,0]
	v_mfma_scale_f32_16x16x128_f8f6f4 v[54:57], v[10:17], v[42:49], 0, v211, v210 op_sel_hi:[0,0,0]
	s_barrier
	s_add_u32 s34, s28, 0x40000
	s_addc_u32 s35, s29, 0
	s_mov_b32 m0, s59
	v_lshl_add_u64 v[2:3], s[34:35], 0, v[188:189]
	global_load_lds_dwordx4 v[2:3], off
	v_lshl_add_u64 v[2:3], s[34:35], 0, v[186:187]
	s_mov_b32 m0, s60
	s_nop 0
	global_load_lds_dwordx4 v[2:3], off
	s_waitcnt vmcnt(6)
	s_barrier
	v_mfma_scale_f32_16x16x128_f8f6f4 v[106:109], v[214:221], v[18:25], 0, v211, v210 op_sel_hi:[0,0,0]
	v_mfma_scale_f32_16x16x128_f8f6f4 v[98:101], v[222:229], v[18:25], 0, v211, v210 op_sel_hi:[0,0,0]
	v_mfma_scale_f32_16x16x128_f8f6f4 v[90:93], v[214:221], v[26:33], 0, v211, v210 op_sel_hi:[0,0,0]
	v_mfma_scale_f32_16x16x128_f8f6f4 v[82:85], v[222:229], v[26:33], 0, v211, v210 op_sel_hi:[0,0,0]
	v_mfma_scale_f32_16x16x128_f8f6f4 v[74:77], v[214:221], v[34:41], 0, v211, v210 op_sel_hi:[0,0,0]
	v_mfma_scale_f32_16x16x128_f8f6f4 v[66:69], v[222:229], v[34:41], 0, v211, v210 op_sel_hi:[0,0,0]
	v_mfma_scale_f32_16x16x128_f8f6f4 v[58:61], v[214:221], v[42:49], 0, v211, v210 op_sel_hi:[0,0,0]
	v_mfma_scale_f32_16x16x128_f8f6f4 v[50:53], v[222:229], v[42:49], 0, v211, v210 op_sel_hi:[0,0,0]
	v_add_u32_e32 v6, s61, v204
	v_add_u32_e32 v14, s61, v205
	s_barrier
	ds_read_b128 v[2:5], v6
	ds_read_b128 v[10:13], v6 offset:2048
	ds_read_b128 v[6:9], v14
	ds_read_b128 v[14:17], v14 offset:2048
	s_mov_b32 m0, s45
	v_lshl_add_u64 v[214:215], s[36:37], 0, v[192:193]
	ds_read_b128 v[18:21], v208 offset:32768
	ds_read_b128 v[26:29], v208 offset:34816
	ds_read_b128 v[22:25], v209 offset:32768
	ds_read_b128 v[30:33], v209 offset:34816
	ds_read_b128 v[34:37], v208 offset:36864
	ds_read_b128 v[42:45], v208 offset:38912
	ds_read_b128 v[38:41], v209 offset:36864
	ds_read_b128 v[46:49], v209 offset:38912
	global_load_lds_dwordx4 v[214:215], off
	v_lshl_add_u64 v[214:215], s[36:37], 0, v[194:195]
	s_mov_b32 m0, s46
	s_nop 0
	global_load_lds_dwordx4 v[214:215], off
	s_waitcnt lgkmcnt(8)
	s_barrier
	s_waitcnt lgkmcnt(0)
	s_waitcnt lgkmcnt(0)
	v_mfma_scale_f32_16x16x128_f8f6f4 v[174:177], v[2:9], v[18:25], v[174:177], v211, v210 op_sel_hi:[0,0,0]
	v_mfma_scale_f32_16x16x128_f8f6f4 v[170:173], v[10:17], v[18:25], v[170:173], v211, v210 op_sel_hi:[0,0,0]
	v_mfma_scale_f32_16x16x128_f8f6f4 v[166:169], v[2:9], v[26:33], v[166:169], v211, v210 op_sel_hi:[0,0,0]
	v_mfma_scale_f32_16x16x128_f8f6f4 v[162:165], v[10:17], v[26:33], v[162:165], v211, v210 op_sel_hi:[0,0,0]
	v_mfma_scale_f32_16x16x128_f8f6f4 v[142:145], v[2:9], v[34:41], v[142:145], v211, v210 op_sel_hi:[0,0,0]
	v_mfma_scale_f32_16x16x128_f8f6f4 v[130:133], v[10:17], v[34:41], v[130:133], v211, v210 op_sel_hi:[0,0,0]
	v_mfma_scale_f32_16x16x128_f8f6f4 v[118:121], v[2:9], v[42:49], v[118:121], v211, v210 op_sel_hi:[0,0,0]
	v_mfma_scale_f32_16x16x128_f8f6f4 v[114:117], v[10:17], v[42:49], v[114:117], v211, v210 op_sel_hi:[0,0,0]
	s_barrier
	s_mov_b32 m0, s63
	v_add_u32_e32 v191, s62, v204
	v_lshl_add_u64 v[230:231], v[230:231], 0, s[12:13]
	v_add_u32_e32 v193, s62, v205
	ds_read_b128 v[214:217], v191
	ds_read_b128 v[222:225], v191 offset:2048
	ds_read_b128 v[218:221], v193
	ds_read_b128 v[226:229], v193 offset:2048
	global_load_lds_dwordx4 v[230:231], off
	v_lshl_add_u64 v[230:231], v[232:233], 0, s[12:13]
	s_add_i32 m0, s63, 0x2000
	s_nop 0
	global_load_lds_dwordx4 v[230:231], off
	s_barrier
	s_waitcnt lgkmcnt(0)
	s_waitcnt lgkmcnt(0)
	v_mfma_scale_f32_16x16x128_f8f6f4 v[158:161], v[214:221], v[18:25], v[158:161], v211, v210 op_sel_hi:[0,0,0]
	v_mfma_scale_f32_16x16x128_f8f6f4 v[154:157], v[222:229], v[18:25], v[154:157], v211, v210 op_sel_hi:[0,0,0]
	v_mfma_scale_f32_16x16x128_f8f6f4 v[150:153], v[214:221], v[26:33], v[150:153], v211, v210 op_sel_hi:[0,0,0]
	v_mfma_scale_f32_16x16x128_f8f6f4 v[146:149], v[222:229], v[26:33], v[146:149], v211, v210 op_sel_hi:[0,0,0]
	v_mfma_scale_f32_16x16x128_f8f6f4 v[138:141], v[214:221], v[34:41], v[138:141], v211, v210 op_sel_hi:[0,0,0]
	v_mfma_scale_f32_16x16x128_f8f6f4 v[134:137], v[222:229], v[34:41], v[134:137], v211, v210 op_sel_hi:[0,0,0]
	v_mfma_scale_f32_16x16x128_f8f6f4 v[126:129], v[214:221], v[42:49], v[126:129], v211, v210 op_sel_hi:[0,0,0]
	v_mfma_scale_f32_16x16x128_f8f6f4 v[122:125], v[222:229], v[42:49], v[122:125], v211, v210 op_sel_hi:[0,0,0]
	s_mov_b32 m0, s49
	v_lshl_add_u64 v[230:231], v[234:235], 0, s[12:13]
	s_barrier
	ds_read_b128 v[18:21], v208 offset:49152
	ds_read_b128 v[26:29], v208 offset:51200
	ds_read_b128 v[22:25], v209 offset:49152
	ds_read_b128 v[30:33], v209 offset:51200
	ds_read_b128 v[34:37], v208 offset:53248
	ds_read_b128 v[42:45], v208 offset:55296
	ds_read_b128 v[38:41], v209 offset:53248
	ds_read_b128 v[46:49], v209 offset:55296
	global_load_lds_dwordx4 v[230:231], off
	v_lshl_add_u64 v[230:231], v[236:237], 0, s[12:13]
	s_mov_b32 m0, s50
	s_nop 0
	global_load_lds_dwordx4 v[230:231], off
	s_barrier
	s_waitcnt lgkmcnt(0)
	s_waitcnt lgkmcnt(0)
	v_mfma_scale_f32_16x16x128_f8f6f4 v[110:113], v[2:9], v[18:25], v[110:113], v211, v210 op_sel_hi:[0,0,0]
	v_mfma_scale_f32_16x16x128_f8f6f4 v[102:105], v[10:17], v[18:25], v[102:105], v211, v210 op_sel_hi:[0,0,0]
	v_mfma_scale_f32_16x16x128_f8f6f4 v[94:97], v[2:9], v[26:33], v[94:97], v211, v210 op_sel_hi:[0,0,0]
	v_mfma_scale_f32_16x16x128_f8f6f4 v[86:89], v[10:17], v[26:33], v[86:89], v211, v210 op_sel_hi:[0,0,0]
	v_mfma_scale_f32_16x16x128_f8f6f4 v[78:81], v[2:9], v[34:41], v[78:81], v211, v210 op_sel_hi:[0,0,0]
	v_mfma_scale_f32_16x16x128_f8f6f4 v[70:73], v[10:17], v[34:41], v[70:73], v211, v210 op_sel_hi:[0,0,0]
	v_mfma_scale_f32_16x16x128_f8f6f4 v[62:65], v[2:9], v[42:49], v[62:65], v211, v210 op_sel_hi:[0,0,0]
	v_mfma_scale_f32_16x16x128_f8f6f4 v[54:57], v[10:17], v[42:49], v[54:57], v211, v210 op_sel_hi:[0,0,0]
	s_barrier
	s_add_u32 s28, s28, 0x40080
	s_addc_u32 s29, s29, 0
	s_add_i32 s34, s62, s40
	v_lshl_add_u64 v[2:3], s[28:29], 0, v[188:189]
	s_mov_b32 m0, s34
	s_nop 0
	global_load_lds_dwordx4 v[2:3], off
	v_lshl_add_u64 v[2:3], s[28:29], 0, v[186:187]
	s_add_i32 m0, s34, 0x2000
	s_nop 0
	global_load_lds_dwordx4 v[2:3], off
	s_waitcnt vmcnt(6)
	s_barrier
	v_mfma_scale_f32_16x16x128_f8f6f4 v[106:109], v[214:221], v[18:25], v[106:109], v211, v210 op_sel_hi:[0,0,0]
	v_mfma_scale_f32_16x16x128_f8f6f4 v[98:101], v[222:229], v[18:25], v[98:101], v211, v210 op_sel_hi:[0,0,0]
	v_mfma_scale_f32_16x16x128_f8f6f4 v[90:93], v[214:221], v[26:33], v[90:93], v211, v210 op_sel_hi:[0,0,0]
	v_mfma_scale_f32_16x16x128_f8f6f4 v[82:85], v[222:229], v[26:33], v[82:85], v211, v210 op_sel_hi:[0,0,0]
	v_mfma_scale_f32_16x16x128_f8f6f4 v[74:77], v[214:221], v[34:41], v[74:77], v211, v210 op_sel_hi:[0,0,0]
	v_mfma_scale_f32_16x16x128_f8f6f4 v[66:69], v[222:229], v[34:41], v[66:69], v211, v210 op_sel_hi:[0,0,0]
	v_mfma_scale_f32_16x16x128_f8f6f4 v[58:61], v[214:221], v[42:49], v[58:61], v211, v210 op_sel_hi:[0,0,0]
	v_mfma_scale_f32_16x16x128_f8f6f4 v[50:53], v[222:229], v[42:49], v[50:53], v211, v210 op_sel_hi:[0,0,0]
	s_cmp_ge_i32 s71, s39
	s_barrier
	s_cbranch_scc1 .LBB0_1546
	s_mov_b64 s[28:29], s[30:31]
	s_branch .LBB0_1551
.LBB0_1551:
	ds_read_b128 v[2:5], v206
	ds_read_b128 v[10:13], v206 offset:2048
	ds_read_b128 v[6:9], v207
	ds_read_b128 v[14:17], v207 offset:2048
	s_cmp_eq_u32 s51, s71
	s_cselect_b64 s[34:35], -1, 0
	s_add_u32 s30, s53, s28
	s_addc_u32 s31, s54, s29
	s_mov_b32 m0, s55
	ds_read_b128 v[26:29], v208
	ds_read_b128 v[18:21], v208 offset:2048
	ds_read_b128 v[30:33], v209
	ds_read_b128 v[22:25], v209 offset:2048
	ds_read_b128 v[42:45], v208 offset:4096
	ds_read_b128 v[34:37], v208 offset:6144
	ds_read_b128 v[46:49], v209 offset:4096
	ds_read_b128 v[38:41], v209 offset:6144
	global_load_lds_dwordx4 v192, s[30:31]
	s_mov_b32 m0, s56
	s_nop 0
	global_load_lds_dwordx4 v194, s[30:31]
	s_waitcnt lgkmcnt(8)
	s_barrier
	s_waitcnt lgkmcnt(0)
	s_barrier
	s_and_b64 s[30:31], s[26:27], s[34:35]
	s_andn2_b64 vcc, exec, s[30:31]
	s_cbranch_vccnz .LBB0_1553
	ds_read2st64_b32 v[190:191], v179 offset1:2
	ds_read2st64_b32 v[192:193], v180 offset1:2
	s_waitcnt lgkmcnt(0)
	v_add_u32_e32 v184, v190, v1
	v_add_u32_e32 v190, v192, v181
	v_add_u32_e32 v192, v191, v1
	v_add_u32_e32 v194, v193, v181
.LBB0_1553:
	s_add_i32 s71, s71, 2
	s_add_u32 s30, s28, 0x100
	s_addc_u32 s31, s29, 0
	s_and_b64 s[36:37], s[34:35], exec
	s_cselect_b32 s36, 0, s30
	s_cselect_b32 s37, 0, s31
	s_add_u32 s36, s22, s36
	s_addc_u32 s37, s23, s37
	s_add_u32 s72, s69, s28
	s_addc_u32 s73, s70, s29
	s_and_b64 s[28:29], s[34:35], exec
	s_cselect_b32 s29, s67, s73
	s_cselect_b32 s28, s68, s72
	s_mov_b32 m0, s42
	v_add_u32_e32 v191, s57, v204
	v_lshl_add_u64 v[230:231], s[28:29], 0, v[188:189]
	v_add_u32_e32 v197, s57, v205
	ds_read_b128 v[214:217], v191
	ds_read_b128 v[222:225], v191 offset:2048
	ds_read_b128 v[218:221], v197
	ds_read_b128 v[226:229], v197 offset:2048
	global_load_lds_dwordx4 v[230:231], off
	v_lshl_add_u64 v[232:233], s[28:29], 0, v[186:187]
	s_mov_b32 m0, s43
	s_waitcnt lgkmcnt(0)
	v_mfma_scale_f32_16x16x128_f8f6f4 v[174:177], v[2:9], v[26:33], v[174:177], v211, v210 op_sel_hi:[0,0,0]
	global_load_lds_dwordx4 v[232:233], off
	s_barrier
	s_waitcnt lgkmcnt(0)
	v_mov_b32_e32 v193, v185
	v_mov_b32_e32 v195, v185
	v_mfma_scale_f32_16x16x128_f8f6f4 v[170:173], v[10:17], v[26:33], v[170:173], v211, v210 op_sel_hi:[0,0,0]
	v_mfma_scale_f32_16x16x128_f8f6f4 v[166:169], v[2:9], v[18:25], v[166:169], v211, v210 op_sel_hi:[0,0,0]
	v_mfma_scale_f32_16x16x128_f8f6f4 v[162:165], v[10:17], v[18:25], v[162:165], v211, v210 op_sel_hi:[0,0,0]
	v_mfma_scale_f32_16x16x128_f8f6f4 v[142:145], v[2:9], v[42:49], v[142:145], v211, v210 op_sel_hi:[0,0,0]
	v_mfma_scale_f32_16x16x128_f8f6f4 v[130:133], v[10:17], v[42:49], v[130:133], v211, v210 op_sel_hi:[0,0,0]
	v_mfma_scale_f32_16x16x128_f8f6f4 v[118:121], v[2:9], v[34:41], v[118:121], v211, v210 op_sel_hi:[0,0,0]
	v_mfma_scale_f32_16x16x128_f8f6f4 v[114:117], v[10:17], v[34:41], v[114:117], v211, v210 op_sel_hi:[0,0,0]
	v_mfma_scale_f32_16x16x128_f8f6f4 v[158:161], v[214:221], v[26:33], v[158:161], v211, v210 op_sel_hi:[0,0,0]
	v_mfma_scale_f32_16x16x128_f8f6f4 v[154:157], v[222:229], v[26:33], v[154:157], v211, v210 op_sel_hi:[0,0,0]
	v_mfma_scale_f32_16x16x128_f8f6f4 v[150:153], v[214:221], v[18:25], v[150:153], v211, v210 op_sel_hi:[0,0,0]
	v_mfma_scale_f32_16x16x128_f8f6f4 v[146:149], v[222:229], v[18:25], v[146:149], v211, v210 op_sel_hi:[0,0,0]
	v_mfma_scale_f32_16x16x128_f8f6f4 v[138:141], v[214:221], v[42:49], v[138:141], v211, v210 op_sel_hi:[0,0,0]
	v_mfma_scale_f32_16x16x128_f8f6f4 v[134:137], v[222:229], v[42:49], v[134:137], v211, v210 op_sel_hi:[0,0,0]
	v_mfma_scale_f32_16x16x128_f8f6f4 v[126:129], v[214:221], v[34:41], v[126:129], v211, v210 op_sel_hi:[0,0,0]
	v_mfma_scale_f32_16x16x128_f8f6f4 v[122:125], v[222:229], v[34:41], v[122:125], v211, v210 op_sel_hi:[0,0,0]
	s_mov_b32 m0, s41
	s_barrier
	ds_read_b128 v[18:21], v208 offset:16384
	ds_read_b128 v[26:29], v208 offset:18432
	ds_read_b128 v[22:25], v209 offset:16384
	ds_read_b128 v[30:33], v209 offset:18432
	ds_read_b128 v[34:37], v208 offset:20480
	ds_read_b128 v[42:45], v208 offset:22528
	ds_read_b128 v[38:41], v209 offset:20480
	ds_read_b128 v[46:49], v209 offset:22528
	global_load_lds_dwordx4 v184, s[36:37]
	s_mov_b32 m0, s44
	v_mov_b32_e32 v191, v185
	global_load_lds_dwordx4 v190, s[36:37]
	s_barrier
	s_waitcnt lgkmcnt(0)
	v_lshl_add_u64 v[234:235], s[36:37], 0, v[184:185]
	v_lshl_add_u64 v[236:237], s[36:37], 0, v[190:191]
	s_waitcnt lgkmcnt(0)
	v_mfma_scale_f32_16x16x128_f8f6f4 v[110:113], v[2:9], v[18:25], v[110:113], v211, v210 op_sel_hi:[0,0,0]
	v_mfma_scale_f32_16x16x128_f8f6f4 v[102:105], v[10:17], v[18:25], v[102:105], v211, v210 op_sel_hi:[0,0,0]
	v_mfma_scale_f32_16x16x128_f8f6f4 v[94:97], v[2:9], v[26:33], v[94:97], v211, v210 op_sel_hi:[0,0,0]
	v_mfma_scale_f32_16x16x128_f8f6f4 v[86:89], v[10:17], v[26:33], v[86:89], v211, v210 op_sel_hi:[0,0,0]
	v_mfma_scale_f32_16x16x128_f8f6f4 v[78:81], v[2:9], v[34:41], v[78:81], v211, v210 op_sel_hi:[0,0,0]
	v_mfma_scale_f32_16x16x128_f8f6f4 v[70:73], v[10:17], v[34:41], v[70:73], v211, v210 op_sel_hi:[0,0,0]
	v_mfma_scale_f32_16x16x128_f8f6f4 v[62:65], v[2:9], v[42:49], v[62:65], v211, v210 op_sel_hi:[0,0,0]
	v_mfma_scale_f32_16x16x128_f8f6f4 v[54:57], v[10:17], v[42:49], v[54:57], v211, v210 op_sel_hi:[0,0,0]
	s_barrier
	s_add_u32 s34, s28, 0x40000
	s_addc_u32 s35, s29, 0
	s_mov_b32 m0, s59
	v_lshl_add_u64 v[2:3], s[34:35], 0, v[188:189]
	global_load_lds_dwordx4 v[2:3], off
	v_lshl_add_u64 v[2:3], s[34:35], 0, v[186:187]
	s_mov_b32 m0, s60
	s_nop 0
	global_load_lds_dwordx4 v[2:3], off
	s_waitcnt vmcnt(6)
	s_barrier
	v_mfma_scale_f32_16x16x128_f8f6f4 v[106:109], v[214:221], v[18:25], v[106:109], v211, v210 op_sel_hi:[0,0,0]
	v_mfma_scale_f32_16x16x128_f8f6f4 v[98:101], v[222:229], v[18:25], v[98:101], v211, v210 op_sel_hi:[0,0,0]
	v_mfma_scale_f32_16x16x128_f8f6f4 v[90:93], v[214:221], v[26:33], v[90:93], v211, v210 op_sel_hi:[0,0,0]
	v_mfma_scale_f32_16x16x128_f8f6f4 v[82:85], v[222:229], v[26:33], v[82:85], v211, v210 op_sel_hi:[0,0,0]
	v_mfma_scale_f32_16x16x128_f8f6f4 v[74:77], v[214:221], v[34:41], v[74:77], v211, v210 op_sel_hi:[0,0,0]
	v_mfma_scale_f32_16x16x128_f8f6f4 v[66:69], v[222:229], v[34:41], v[66:69], v211, v210 op_sel_hi:[0,0,0]
	v_mfma_scale_f32_16x16x128_f8f6f4 v[58:61], v[214:221], v[42:49], v[58:61], v211, v210 op_sel_hi:[0,0,0]
	v_mfma_scale_f32_16x16x128_f8f6f4 v[50:53], v[222:229], v[42:49], v[50:53], v211, v210 op_sel_hi:[0,0,0]
	v_add_u32_e32 v6, s61, v204
	v_add_u32_e32 v14, s61, v205
	s_barrier
	ds_read_b128 v[2:5], v6
	ds_read_b128 v[10:13], v6 offset:2048
	ds_read_b128 v[6:9], v14
	ds_read_b128 v[14:17], v14 offset:2048
	s_mov_b32 m0, s45
	v_lshl_add_u64 v[214:215], s[36:37], 0, v[192:193]
	ds_read_b128 v[18:21], v208 offset:32768
	ds_read_b128 v[26:29], v208 offset:34816
	ds_read_b128 v[22:25], v209 offset:32768
	ds_read_b128 v[30:33], v209 offset:34816
	ds_read_b128 v[34:37], v208 offset:36864
	ds_read_b128 v[42:45], v208 offset:38912
	ds_read_b128 v[38:41], v209 offset:36864
	ds_read_b128 v[46:49], v209 offset:38912
	global_load_lds_dwordx4 v[214:215], off
	v_lshl_add_u64 v[214:215], s[36:37], 0, v[194:195]
	s_mov_b32 m0, s46
	s_nop 0
	global_load_lds_dwordx4 v[214:215], off
	s_waitcnt lgkmcnt(8)
	s_barrier
	s_waitcnt lgkmcnt(0)
	s_waitcnt lgkmcnt(0)
	v_mfma_scale_f32_16x16x128_f8f6f4 v[174:177], v[2:9], v[18:25], v[174:177], v211, v210 op_sel_hi:[0,0,0]
	v_mfma_scale_f32_16x16x128_f8f6f4 v[170:173], v[10:17], v[18:25], v[170:173], v211, v210 op_sel_hi:[0,0,0]
	v_mfma_scale_f32_16x16x128_f8f6f4 v[166:169], v[2:9], v[26:33], v[166:169], v211, v210 op_sel_hi:[0,0,0]
	v_mfma_scale_f32_16x16x128_f8f6f4 v[162:165], v[10:17], v[26:33], v[162:165], v211, v210 op_sel_hi:[0,0,0]
	v_mfma_scale_f32_16x16x128_f8f6f4 v[142:145], v[2:9], v[34:41], v[142:145], v211, v210 op_sel_hi:[0,0,0]
	v_mfma_scale_f32_16x16x128_f8f6f4 v[130:133], v[10:17], v[34:41], v[130:133], v211, v210 op_sel_hi:[0,0,0]
	v_mfma_scale_f32_16x16x128_f8f6f4 v[118:121], v[2:9], v[42:49], v[118:121], v211, v210 op_sel_hi:[0,0,0]
	v_mfma_scale_f32_16x16x128_f8f6f4 v[114:117], v[10:17], v[42:49], v[114:117], v211, v210 op_sel_hi:[0,0,0]
	s_barrier
	s_mov_b32 m0, s63
	v_add_u32_e32 v191, s62, v204
	v_lshl_add_u64 v[230:231], v[230:231], 0, s[12:13]
	v_add_u32_e32 v193, s62, v205
	ds_read_b128 v[214:217], v191
	ds_read_b128 v[222:225], v191 offset:2048
	ds_read_b128 v[218:221], v193
	ds_read_b128 v[226:229], v193 offset:2048
	global_load_lds_dwordx4 v[230:231], off
	v_lshl_add_u64 v[230:231], v[232:233], 0, s[12:13]
	s_add_i32 m0, s63, 0x2000
	s_nop 0
	global_load_lds_dwordx4 v[230:231], off
	s_barrier
	s_waitcnt lgkmcnt(0)
	s_waitcnt lgkmcnt(0)
	v_mfma_scale_f32_16x16x128_f8f6f4 v[158:161], v[214:221], v[18:25], v[158:161], v211, v210 op_sel_hi:[0,0,0]
	v_mfma_scale_f32_16x16x128_f8f6f4 v[154:157], v[222:229], v[18:25], v[154:157], v211, v210 op_sel_hi:[0,0,0]
	v_mfma_scale_f32_16x16x128_f8f6f4 v[150:153], v[214:221], v[26:33], v[150:153], v211, v210 op_sel_hi:[0,0,0]
	v_mfma_scale_f32_16x16x128_f8f6f4 v[146:149], v[222:229], v[26:33], v[146:149], v211, v210 op_sel_hi:[0,0,0]
	v_mfma_scale_f32_16x16x128_f8f6f4 v[138:141], v[214:221], v[34:41], v[138:141], v211, v210 op_sel_hi:[0,0,0]
	v_mfma_scale_f32_16x16x128_f8f6f4 v[134:137], v[222:229], v[34:41], v[134:137], v211, v210 op_sel_hi:[0,0,0]
	v_mfma_scale_f32_16x16x128_f8f6f4 v[126:129], v[214:221], v[42:49], v[126:129], v211, v210 op_sel_hi:[0,0,0]
	v_mfma_scale_f32_16x16x128_f8f6f4 v[122:125], v[222:229], v[42:49], v[122:125], v211, v210 op_sel_hi:[0,0,0]
	s_mov_b32 m0, s49
	v_lshl_add_u64 v[230:231], v[234:235], 0, s[12:13]
	s_barrier
	ds_read_b128 v[18:21], v208 offset:49152
	ds_read_b128 v[26:29], v208 offset:51200
	ds_read_b128 v[22:25], v209 offset:49152
	ds_read_b128 v[30:33], v209 offset:51200
	ds_read_b128 v[34:37], v208 offset:53248
	ds_read_b128 v[42:45], v208 offset:55296
	ds_read_b128 v[38:41], v209 offset:53248
	ds_read_b128 v[46:49], v209 offset:55296
	global_load_lds_dwordx4 v[230:231], off
	v_lshl_add_u64 v[230:231], v[236:237], 0, s[12:13]
	s_mov_b32 m0, s50
	s_nop 0
	global_load_lds_dwordx4 v[230:231], off
	s_barrier
	s_waitcnt lgkmcnt(0)
	s_waitcnt lgkmcnt(0)
	v_mfma_scale_f32_16x16x128_f8f6f4 v[110:113], v[2:9], v[18:25], v[110:113], v211, v210 op_sel_hi:[0,0,0]
	v_mfma_scale_f32_16x16x128_f8f6f4 v[102:105], v[10:17], v[18:25], v[102:105], v211, v210 op_sel_hi:[0,0,0]
	v_mfma_scale_f32_16x16x128_f8f6f4 v[94:97], v[2:9], v[26:33], v[94:97], v211, v210 op_sel_hi:[0,0,0]
	v_mfma_scale_f32_16x16x128_f8f6f4 v[86:89], v[10:17], v[26:33], v[86:89], v211, v210 op_sel_hi:[0,0,0]
	v_mfma_scale_f32_16x16x128_f8f6f4 v[78:81], v[2:9], v[34:41], v[78:81], v211, v210 op_sel_hi:[0,0,0]
	v_mfma_scale_f32_16x16x128_f8f6f4 v[70:73], v[10:17], v[34:41], v[70:73], v211, v210 op_sel_hi:[0,0,0]
	v_mfma_scale_f32_16x16x128_f8f6f4 v[62:65], v[2:9], v[42:49], v[62:65], v211, v210 op_sel_hi:[0,0,0]
	v_mfma_scale_f32_16x16x128_f8f6f4 v[54:57], v[10:17], v[42:49], v[54:57], v211, v210 op_sel_hi:[0,0,0]
	s_barrier
	s_add_u32 s28, s28, 0x40080
	s_addc_u32 s29, s29, 0
	s_add_i32 s34, s62, s40
	v_lshl_add_u64 v[2:3], s[28:29], 0, v[188:189]
	s_mov_b32 m0, s34
	s_nop 0
	global_load_lds_dwordx4 v[2:3], off
	v_lshl_add_u64 v[2:3], s[28:29], 0, v[186:187]
	s_add_i32 m0, s34, 0x2000
	s_nop 0
	global_load_lds_dwordx4 v[2:3], off
	s_waitcnt vmcnt(6)
	s_barrier
	v_mfma_scale_f32_16x16x128_f8f6f4 v[106:109], v[214:221], v[18:25], v[106:109], v211, v210 op_sel_hi:[0,0,0]
	v_mfma_scale_f32_16x16x128_f8f6f4 v[98:101], v[222:229], v[18:25], v[98:101], v211, v210 op_sel_hi:[0,0,0]
	v_mfma_scale_f32_16x16x128_f8f6f4 v[90:93], v[214:221], v[26:33], v[90:93], v211, v210 op_sel_hi:[0,0,0]
	v_mfma_scale_f32_16x16x128_f8f6f4 v[82:85], v[222:229], v[26:33], v[82:85], v211, v210 op_sel_hi:[0,0,0]
	v_mfma_scale_f32_16x16x128_f8f6f4 v[74:77], v[214:221], v[34:41], v[74:77], v211, v210 op_sel_hi:[0,0,0]
	v_mfma_scale_f32_16x16x128_f8f6f4 v[66:69], v[222:229], v[34:41], v[66:69], v211, v210 op_sel_hi:[0,0,0]
	v_mfma_scale_f32_16x16x128_f8f6f4 v[58:61], v[214:221], v[42:49], v[58:61], v211, v210 op_sel_hi:[0,0,0]
	v_mfma_scale_f32_16x16x128_f8f6f4 v[50:53], v[222:229], v[42:49], v[50:53], v211, v210 op_sel_hi:[0,0,0]
	s_cmp_ge_i32 s71, s39
	s_barrier
	s_cbranch_scc1 .LBB0_1546
	s_mov_b64 s[28:29], s[30:31]
	s_branch .LBB0_1551
